# idle-slot filling: workgroups without a 5th RG-LRU item convert 2 deferred weight tiles at the end of phase 3 (re-instantiated conversion loop); deferral 2800+1480 tiles
# speedup vs baseline: 1.0000x; 1.0000x over previous
; __device__ __forceinline__ void bt_load(const float* __restrict__ src, int N, int perm, int it, int ntn, f32x4 (&v)[8]) {
;     const int wid = threadIdx.x >> 6, lane = threadIdx.x & 63;
;     const int per = 16 * ntn, z = it / per, r = it % per, kt = r / ntn, nt = r % ntn;
;     const int np = nt * 256 + lane * 4;
;     const int sc = perm ? (nt * 128 + (lane & 31) * 4 + (lane >> 5) * 1024) : np;
;     const float* p = src + (size_t)z * 1024 * N + (size_t)(kt * 64 + wid * 8) * N + sc;
; #pragma unroll
;     for (int i = 0; i < 8; ++i) v[i] = __builtin_nontemporal_load((const f32x4*)(p + (size_t)i * N));
; }
; __device__ __forceinline__ void ph_big_transpose(const float* __restrict__ src, int N, int perm, int batch, bf16* __restrict__ dst, float* tile  , int G, int ndefer) {
;     const int tid = threadIdx.x, wid = tid >> 6, lane = tid & 63, ntn = N / 256, total = batch * 16 * ntn - ndefer;
;     int it = (int)blockIdx.x;
;     if (it >= total) return;
;     f32x4 cur[8], nxt[8], nx2[8];
;     bt_load(src, N, perm, it, ntn, cur);
;     if (it + G < total) bt_load(src, N, perm, it + G, ntn, nxt);
;     for (; it < total; it += G) {
;         const bool more = it + G < total, more2 = it + 2 * G < total;
;         if (more2) bt_load(src, N, perm, it + 2 * G, ntn, nx2);
.LBB0_71:
	s_cmpk_gt_i32 s2, 0xa37
	s_cbranch_scc1 .LBB0_79
	s_ashr_i32 s0, s2, 31
	s_lshr_b32 s0, s0, 26
	s_add_i32 s1, s2, s0
	s_ashr_i32 s0, s1, 6
	s_and_b32 s1, s1, 0xffc0
	s_sub_i32 s1, s2, s1
	s_bfe_i32 s4, s1, 0x80000
	s_bfe_u32 s4, s4, 0x2000d
	s_add_i32 s4, s1, s4
	s_bfe_i32 s5, s4, 0x80000
	s_and_b32 s4, s4, 0xfc
	s_sub_i32 s1, s1, s4
	v_lshlrev_b32_e32 v2, 2, v0
	s_sext_i32_i8 s1, s1
	v_and_b32_e32 v99, 0xfc, v2
	v_lshl_or_b32 v2, s1, 8, v99
	s_ashr_i32 s1, s0, 31
	s_lshl_b64 s[0:1], s[0:1], 22
	s_sext_i32_i16 s5, s5
	s_add_u32 s0, s72, s0
	s_addc_u32 s1, s73, s1
	s_lshl_b32 s4, s5, 4
	v_lshrrev_b32_e32 v3, 3, v0
	s_andn2_b32 s4, s4, 63
	v_and_b32_e32 v110, 56, v3
	v_or_b32_e32 v4, s4, v110
	v_ashrrev_i32_e32 v5, 31, v4
	v_lshlrev_b64 v[4:5], 12, v[4:5]
	v_lshl_add_u64 v[4:5], s[0:1], 0, v[4:5]
	v_ashrrev_i32_e32 v3, 31, v2
	v_lshl_add_u64 v[2:3], v[2:3], 2, v[4:5]
	s_movk_i32 s0, 0x2000
	v_add_co_u32_e32 v4, vcc, s0, v2
	s_movk_i32 s4, 0x4000
	s_nop 0
	v_addc_co_u32_e32 v5, vcc, 0, v3, vcc
	global_load_dwordx4 v[42:45], v[4:5], off offset:-4096 nt
	global_load_dwordx4 v[34:37], v[4:5], off nt
	v_add_co_u32_e32 v4, vcc, s4, v2
	s_movk_i32 s1, 0x5000
	s_nop 0
	v_addc_co_u32_e32 v5, vcc, 0, v3, vcc
	global_load_dwordx4 v[46:49], v[4:5], off offset:-4096 nt
	global_load_dwordx4 v[38:41], v[4:5], off nt
	v_add_co_u32_e32 v4, vcc, s1, v2
	s_add_i32 s5, s62, s2
	s_nop 0
	v_addc_co_u32_e32 v5, vcc, 0, v3, vcc
	global_load_dwordx4 v[62:65], v[2:3], off nt
	global_load_dwordx4 v[50:53], v[4:5], off nt
	v_add_co_u32_e32 v4, vcc, 0x6000, v2
	s_cmpk_gt_i32 s5, 0xa37
	s_nop 0
	v_addc_co_u32_e32 v5, vcc, 0, v3, vcc
	v_add_co_u32_e32 v2, vcc, 0x7000, v2
	s_movk_i32 s1, 0x3000
	s_nop 0
	v_addc_co_u32_e32 v3, vcc, 0, v3, vcc
	global_load_dwordx4 v[58:61], v[4:5], off nt
	global_load_dwordx4 v[54:57], v[2:3], off nt
	s_cbranch_scc1 .LBB0_74
	s_ashr_i32 s6, s5, 31
	s_lshr_b32 s6, s6, 26
	s_add_i32 s7, s5, s6
	s_ashr_i32 s6, s7, 6
	s_and_b32 s7, s7, 0xffc0
	s_sub_i32 s5, s5, s7
	s_bfe_i32 s7, s5, 0x80000
	s_bfe_u32 s7, s7, 0x2000d
	s_add_i32 s7, s5, s7
	s_bfe_i32 s8, s7, 0x80000
	s_and_b32 s7, s7, 0xfc
	s_sub_i32 s5, s5, s7
	s_ashr_i32 s7, s6, 31
	s_lshl_b64 s[6:7], s[6:7], 22
	s_sext_i32_i16 s8, s8
	s_sext_i32_i8 s5, s5
	s_add_u32 s6, s72, s6
	v_lshl_or_b32 v2, s5, 8, v99
	s_addc_u32 s7, s73, s7
	s_lshl_b32 s5, s8, 4
	s_andn2_b32 s5, s5, 63
	v_or_b32_e32 v4, s5, v110
	v_ashrrev_i32_e32 v5, 31, v4
	v_lshlrev_b64 v[4:5], 12, v[4:5]
	v_lshl_add_u64 v[4:5], s[6:7], 0, v[4:5]
	v_ashrrev_i32_e32 v3, 31, v2
	v_lshl_add_u64 v[26:27], v[2:3], 2, v[4:5]
	v_add_co_u32_e32 v2, vcc, s0, v26
	s_nop 1
	v_addc_co_u32_e32 v3, vcc, 0, v27, vcc
	v_add_co_u32_e32 v10, vcc, s4, v26
	global_load_dwordx4 v[6:9], v[2:3], off offset:-4096 nt
	s_nop 0
	global_load_dwordx4 v[2:5], v[2:3], off nt
	v_addc_co_u32_e32 v11, vcc, 0, v27, vcc
	v_add_co_u32_e32 v18, vcc, 0x5000, v26
	global_load_dwordx4 v[14:17], v[10:11], off offset:-4096 nt
	s_nop 0
	global_load_dwordx4 v[10:13], v[10:11], off nt
	v_addc_co_u32_e32 v19, vcc, 0, v27, vcc
	v_add_co_u32_e32 v28, vcc, 0x6000, v26
	global_load_dwordx4 v[22:25], v[26:27], off nt
	s_nop 0
	global_load_dwordx4 v[18:21], v[18:19], off nt
	v_addc_co_u32_e32 v29, vcc, 0, v27, vcc
	v_add_co_u32_e32 v30, vcc, 0x7000, v26
	s_nop 1
	v_addc_co_u32_e32 v31, vcc, 0, v27, vcc
	global_load_dwordx4 v[26:29], v[28:29], off nt
	s_nop 0
	global_load_dwordx4 v[30:33], v[30:31], off nt

; __device__ __forceinline__ unsigned g8_cvt_pk(float lo, float hi) { unsigned r; asm volatile("v_cvt_pk_bf16_f32 %0, %1, %2" : "=v"(r) : "v"(lo), "v"(hi)); return r; }
; __device__ __forceinline__ void ph_big_transpose(const float* __restrict__ src, int N, int perm, int batch, bf16* __restrict__ dst, float* tile  , int G, int ndefer) {
;     ...
;     for (; it < total; it += G) {
;         const bool more = it + G < total, more2 = it + 2 * G < total;
;         if (more2) bt_load(src, N, perm, it + 2 * G, ntn, nx2);
;         __syncthreads();
; #pragma unroll
;         for (int i = 0; i < 8; ++i) { float* t = tile + (wid * 8 + i) * 257 + lane * 4; t[0] = cur[i][0]; t[1] = cur[i][1]; t[2] = cur[i][2]; t[3] = cur[i][3]; }
;         __syncthreads();
;         const int per = 16 * ntn, z = it / per, r = it % per, kt = r / ntn, nt = r % ntn;
;         bf16* d = dst + (size_t)z * N * 1024 + (((size_t)nt * 16 + kt) << 14);
;         const int kc = lane & 7;
; #pragma unroll
;         for (int pss = 0; pss < 4; ++pss) {
;             const int n = wid * 32 + pss * 8 + (lane >> 3); float f[8];
; #pragma unroll
;             for (int j = 0; j < 8; ++j) f[j] = tile[(kc * 8 + j) * 257 + n];
;             u32x4 w; w.x = g8_cvt_pk(f[0], f[1]); w.y = g8_cvt_pk(f[2], f[3]); w.z = g8_cvt_pk(f[4], f[5]); w.w = g8_cvt_pk(f[6], f[7]);
;             __builtin_nontemporal_store(w, (u32x4*)(d + n * 64 + kc * 8));
;         }
;         if (more) {
; #pragma unroll
;             for (int i = 0; i < 8; ++i) { cur[i] = nxt[i]; nxt[i] = nx2[i]; } }
;     }
.LBB0_75:
	s_ashr_i32 s8, s3, 31
	s_barrier
	s_waitcnt vmcnt(3)
	ds_write_b128 v111, v[62:65]
	v_add_u32_e32 v62, 0x404, v111
	s_lshr_b32 s8, s8, 26
	ds_write2_b32 v62, v42, v43 offset1:1
	v_add_u32_e32 v42, 0x40c, v111
	s_add_i32 s9, s3, s8
	ds_write2_b32 v42, v44, v45 offset1:1
	v_add_u32_e32 v42, 0x808, v111
	s_ashr_i32 s8, s9, 6
	s_and_b32 s9, s9, 0xffc0
	s_add_i32 s7, s3, s62
	ds_write2_b64 v42, v[34:35], v[36:37] offset1:1
	v_add_u32_e32 v34, 0xc0c, v111
	s_sub_i32 s3, s3, s9
	ds_write2_b32 v34, v46, v47 offset1:1
	v_add_u32_e32 v34, 0xc14, v111
	s_bfe_i32 s9, s3, 0x80000
	ds_write2_b32 v34, v48, v49 offset1:1
	ds_write_b128 v111, v[38:41] offset:4112
	v_add_u32_e32 v34, 0x1414, v111
	s_bfe_u32 s9, s9, 0x2000d
	s_waitcnt vmcnt(2)
	ds_write2_b32 v34, v50, v51 offset1:1
	v_add_u32_e32 v34, 0x141c, v111
	s_add_i32 s9, s3, s9
	ds_write2_b32 v34, v52, v53 offset1:1
	v_add_u32_e32 v34, 0x1818, v111
	s_bfe_i32 s10, s9, 0x80000
	s_and_b32 s9, s9, 0xfc
	s_waitcnt vmcnt(1)
	ds_write2_b64 v34, v[58:59], v[60:61] offset1:1
	v_add_u32_e32 v34, 0x1c1c, v111
	s_sext_i32_i16 s10, s10
	s_sub_i32 s30, s3, s9
	s_ashr_i32 s9, s8, 31
	s_waitcnt vmcnt(0)
	ds_write2_b32 v34, v54, v55 offset1:1
	v_add_u32_e32 v34, 0x1c24, v111
	s_lshr_b32 s10, s10, 2
	s_lshl_b64 s[8:9], s[8:9], 21
	ds_write2_b32 v34, v56, v57 offset1:1
	s_waitcnt lgkmcnt(0)
	s_barrier
	s_add_u32 s3, s4, s8
	ds_read_b32 v34, v112 offset:1028
	ds_read_b32 v35, v112 offset:3084
	ds_read_b32 v36, v112 offset:5140
	ds_read_b32 v37, v112 offset:7196
	ds_read_b32 v38, v112 offset:6168
	ds_read_b32 v39, v112 offset:4112
	ds_read_b32 v40, v112 offset:2056
	ds_read_b32 v41, v112
	s_addc_u32 s31, s5, s9
	s_bfe_i64 s[8:9], s[30:31], 0x80000
	s_bfe_i64 s[10:11], s[10:11], 0x100000
	s_lshl_b64 s[8:9], s[8:9], 19
	s_add_u32 s3, s3, s8
	s_addc_u32 s30, s31, s9
	s_lshl_b64 s[8:9], s[10:11], 15
	s_waitcnt lgkmcnt(0)
	v_cvt_pk_bf16_f32 v34, v41, v34
	v_cvt_pk_bf16_f32 v35, v40, v35
	v_cvt_pk_bf16_f32 v36, v39, v36
	v_cvt_pk_bf16_f32 v37, v38, v37
	ds_read_b32 v42, v112 offset:1060
	ds_read_b32 v43, v112 offset:3116
	ds_read_b32 v44, v112 offset:5172
	ds_read_b32 v45, v112 offset:7228
	ds_read_b32 v46, v112 offset:6200
	ds_read_b32 v47, v112 offset:4144
	ds_read_b32 v48, v112 offset:2088
	ds_read_b32 v49, v112 offset:32
	s_add_u32 s8, s3, s8
	s_addc_u32 s9, s30, s9
	v_lshl_add_u64 v[38:39], s[8:9], 0, v[100:101]
	v_mov_b32_e32 v103, v101
	v_lshl_add_u64 v[40:41], v[38:39], 0, v[102:103]
	global_store_dwordx4 v[40:41], v[34:37], off nt
	v_mov_b32_e32 v105, v101
	v_lshl_add_u64 v[40:41], v[38:39], 0, v[104:105]
	s_waitcnt lgkmcnt(0)
	v_cvt_pk_bf16_f32 v34, v49, v42
	v_cvt_pk_bf16_f32 v35, v48, v43
	v_cvt_pk_bf16_f32 v36, v47, v44
	v_cvt_pk_bf16_f32 v37, v46, v45
	ds_read_b32 v42, v112 offset:1092
	ds_read_b32 v43, v112 offset:3148
	ds_read_b32 v44, v112 offset:5204
	ds_read_b32 v45, v112 offset:6232
	ds_read_b32 v46, v112 offset:4176
	ds_read_b32 v47, v112 offset:2120
	ds_read_b32 v48, v112 offset:64
	ds_read_b32 v49, v112 offset:7260
	global_store_dwordx4 v[40:41], v[34:37], off nt
	v_mov_b32_e32 v107, v101
	v_lshl_add_u64 v[40:41], v[38:39], 0, v[106:107]
	s_waitcnt lgkmcnt(1)
	v_cvt_pk_bf16_f32 v34, v48, v42
	v_cvt_pk_bf16_f32 v35, v47, v43
	v_cvt_pk_bf16_f32 v36, v46, v44
	s_waitcnt lgkmcnt(0)
	v_cvt_pk_bf16_f32 v37, v45, v49
	ds_read_b32 v42, v112 offset:1124
	ds_read_b32 v43, v112 offset:3180
	ds_read_b32 v44, v112 offset:5236
	ds_read_b32 v45, v112 offset:6264
	ds_read_b32 v46, v112 offset:4208
	ds_read_b32 v47, v112 offset:2152
	ds_read_b32 v48, v112 offset:96
	ds_read_b32 v49, v112 offset:7292
	v_mov_b32_e32 v109, v101
	global_store_dwordx4 v[40:41], v[34:37], off nt
	v_lshl_add_u64 v[38:39], v[38:39], 0, v[108:109]
	v_mov_b64_e32 v[56:57], v[32:33]
	s_waitcnt lgkmcnt(1)
	v_cvt_pk_bf16_f32 v34, v48, v42
	v_cvt_pk_bf16_f32 v35, v47, v43
	v_cvt_pk_bf16_f32 v36, v46, v44
	s_waitcnt lgkmcnt(0)
	v_cvt_pk_bf16_f32 v37, v45, v49
	global_store_dwordx4 v[38:39], v[34:37], off nt
	v_mov_b64_e32 v[60:61], v[28:29]
	v_mov_b64_e32 v[52:53], v[20:21]
	v_mov_b64_e32 v[40:41], v[12:13]
	v_mov_b64_e32 v[48:49], v[16:17]
	v_mov_b64_e32 v[36:37], v[4:5]
	v_mov_b64_e32 v[44:45], v[8:9]
	v_mov_b64_e32 v[64:65], v[24:25]
	v_mov_b64_e32 v[54:55], v[30:31]
	v_mov_b64_e32 v[58:59], v[26:27]
	v_mov_b64_e32 v[50:51], v[18:19]
	v_mov_b64_e32 v[38:39], v[10:11]
	v_mov_b64_e32 v[46:47], v[14:15]
	v_mov_b64_e32 v[34:35], v[2:3]
	v_mov_b64_e32 v[42:43], v[6:7]
	v_mov_b64_e32 v[62:63], v[22:23]
	v_mov_b64_e32 v[30:31], v[94:95]
	v_mov_b64_e32 v[26:27], v[90:91]
	v_mov_b64_e32 v[18:19], v[86:87]
	v_mov_b64_e32 v[10:11], v[82:83]
	v_mov_b64_e32 v[14:15], v[74:75]
	v_mov_b64_e32 v[2:3], v[66:67]
	v_mov_b64_e32 v[6:7], v[70:71]
	v_mov_b64_e32 v[22:23], v[78:79]
	s_cmpk_lt_i32 s7, 0xa38
	v_mov_b64_e32 v[32:33], v[96:97]
	v_mov_b64_e32 v[28:29], v[92:93]
	v_mov_b64_e32 v[20:21], v[88:89]
	v_mov_b64_e32 v[12:13], v[84:85]
	v_mov_b64_e32 v[16:17], v[76:77]
	v_mov_b64_e32 v[4:5], v[68:69]
	v_mov_b64_e32 v[8:9], v[72:73]
	v_mov_b64_e32 v[24:25], v[80:81]
	s_mov_b32 s3, s7
	s_cbranch_scc0 .LBB0_78
.LBB0_76:
	s_add_i32 s7, s6, s3
	s_cmpk_gt_i32 s7, 0xa37
	s_cbranch_scc1 .LBB0_75
	s_ashr_i32 s8, s7, 31
	s_lshr_b32 s8, s8, 26
	s_add_i32 s9, s7, s8
	s_ashr_i32 s8, s9, 6
	s_and_b32 s9, s9, 0xffc0
	s_sub_i32 s7, s7, s9
	s_bfe_i32 s9, s7, 0x80000
	s_bfe_u32 s9, s9, 0x2000d
	s_add_i32 s9, s7, s9
	s_bfe_i32 s10, s9, 0x80000
	s_and_b32 s9, s9, 0xfc
	s_sub_i32 s7, s7, s9
	s_ashr_i32 s9, s8, 31
	s_lshl_b64 s[8:9], s[8:9], 22
	s_sext_i32_i16 s10, s10
	s_sext_i32_i8 s7, s7
	s_add_u32 s8, s72, s8
	v_lshl_or_b32 v66, s7, 8, v99
	s_addc_u32 s9, s73, s9
	s_lshl_b32 s7, s10, 4
	s_andn2_b32 s7, s7, 63
	v_or_b32_e32 v68, s7, v110
	v_ashrrev_i32_e32 v69, 31, v68
	v_lshlrev_b64 v[68:69], 12, v[68:69]
	v_lshl_add_u64 v[68:69], s[8:9], 0, v[68:69]
	v_ashrrev_i32_e32 v67, 31, v66
	v_lshl_add_u64 v[90:91], v[66:67], 2, v[68:69]
	v_add_co_u32_e32 v66, vcc, s0, v90
	s_nop 1
	v_addc_co_u32_e32 v67, vcc, 0, v91, vcc
	v_add_co_u32_e32 v74, vcc, s1, v90
	global_load_dwordx4 v[70:73], v[66:67], off offset:-4096 nt
	s_nop 0
	global_load_dwordx4 v[66:69], v[66:67], off nt
	v_addc_co_u32_e32 v75, vcc, 0, v91, vcc
	v_add_co_u32_e32 v82, vcc, 0x4000, v90
	global_load_dwordx4 v[78:81], v[90:91], off nt
	s_nop 0
	global_load_dwordx4 v[74:77], v[74:75], off nt
	v_addc_co_u32_e32 v83, vcc, 0, v91, vcc
	v_add_co_u32_e32 v86, vcc, 0x5000, v90
	s_nop 1
	v_addc_co_u32_e32 v87, vcc, 0, v91, vcc
	v_add_co_u32_e32 v92, vcc, 0x6000, v90
	global_load_dwordx4 v[82:85], v[82:83], off nt
	s_nop 0
	global_load_dwordx4 v[86:89], v[86:87], off nt
	v_addc_co_u32_e32 v93, vcc, 0, v91, vcc
	v_add_co_u32_e32 v94, vcc, 0x7000, v90
	s_nop 1
	v_addc_co_u32_e32 v95, vcc, 0, v91, vcc
	global_load_dwordx4 v[90:93], v[92:93], off nt
	s_nop 0
	global_load_dwordx4 v[94:97], v[94:95], off nt
	s_branch .LBB0_75

; #define SEAM(k) do { if (IN(k) && IN((k) + 1)) xcd_barrier(bar); \
;         if (PROBE_MASK) { const unsigned long long t_ = __builtin_amdgcn_s_memrealtime(); if ((PROBE_MASK >> (k)) & 1u) pr_acc += t_ - pr_t0; pr_t0 = t_; } } while (0)
; __device__ __forceinline__ void convert_deferred(const Ptrs& P, unsigned char* lds, int quota) {
;     const int tid = threadIdx.x, wid = tid >> 6, lane = tid & 63;
;     float* tile = (float*)lds;
;     volatile __attribute__((address_space(3))) int* slot = (volatile __attribute__((address_space(3))) int*)((__attribute__((address_space(3))) unsigned char*)lds + 131072 + 320 + 11000);
;     unsigned* q = (unsigned*)(P.ws + WS_CTL) + CW_DEFQ;
;     for (int n = 0; n < quota; ++n) {
;         __syncthreads();
;         if (tid == 0) *slot = (int)atomicAdd(q, 1u);
;         __syncthreads();
;         const int t = *slot;
;         if (t >= DEF_GU + DEF_DN) break;
;         const bool gu = t < DEF_GU;
;         const float* src = gu ? P.in[34] : P.in[36]; bf16* dst = (bf16*)(P.ws + (gu ? WS_WGU : WS_WDN));
;         const int N = gu ? 2048 : 1024, ntn = N / 256, it = gu ? 2 * NE * 16 * 8 - DEF_GU + t : 2 * NE * 16 * 4 - DEF_DN + (t - DEF_GU);
; __global__ void __launch_bounds__(NT, 2) mega(Args args) {
;     ...
;     if (IN(2)) { g8::DenseOrder S; S.init(H, D, (const bf16*)(ws + WS_WEVIN), D, R, EVEN_IN_P, G, (int)blockIdx.x, 0); g8::EpiStoreBf16 E{Z, EVEN_IN_P};
;         g8::gemm_phase<g8::EpiStoreBf16, g8::DenseOrder, false, true>(LDSP, D, D, S, E);
;         if (IDLE_LAST(68 * 7)) convert_deferred(P, lds, 4); } SEAM(2);
.LBB0_779:
	s_abs_i32 s3, s62
	v_cvt_f32_u32_e32 v2, s3
	s_sub_i32 s4, 0, s3
	s_mov_b32 s5, 0
	v_rcp_iflag_f32_e32 v2, v2
	s_nop 0
	v_mul_f32_e32 v2, 0x4f7ffffe, v2
	v_cvt_u32_f32_e32 v2, v2
	s_nop 0
	v_readfirstlane_b32 s6, v2
	s_mul_i32 s4, s4, s6
	s_mul_hi_u32 s4, s6, s4
	s_add_i32 s6, s6, s4
	s_mul_hi_u32 s4, s6, 0x1dc
	s_mul_i32 s4, s4, s3
	s_sub_i32 s4, 0x1dc, s4
	s_sub_i32 s6, s4, s3
	s_cmp_ge_u32 s4, s3
	s_cselect_b32 s4, s6, s4
	s_sub_i32 s6, s4, s3
	s_cmp_ge_u32 s4, s3
	s_cselect_b32 s3, s6, s4
	s_cmp_eq_u32 s3, 0
	s_cselect_b64 s[6:7], -1, 0
	s_cmp_lt_i32 s2, s3
	s_cselect_b64 s[8:9], -1, 0
	s_or_b64 s[6:7], s[6:7], s[8:9]
	s_and_b64 vcc, exec, s[6:7]
	s_cbranch_vccnz .LBB0_789
	v_and_b32_e32 v2, 0x7c, v155
	v_lshlrev_b32_e32 v3, 5, v0
	s_movk_i32 s3, 0x400
	v_lshrrev_b32_e32 v4, 6, v0
	v_and_or_b32 v12, v3, s3, v2
	v_bfe_u32 v2, v0, 3, 3
	v_lshl_or_b32 v5, v4, 5, v2
	v_lshlrev_b32_e32 v2, 3, v0
	v_lshl_add_u32 v11, v182, 4, 0
	v_and_b32_e32 v2, 56, v2
	v_mul_u32_u24_e32 v16, 0x2020, v4
	v_mov_b32_e32 v3, 0
	v_lshl_add_u32 v27, v5, 2, 0
	v_mul_u32_u24_e32 v28, 0x404, v2
	v_lshlrev_b32_e32 v10, 6, v5
	s_add_i32 s12, 0, 0x22c38
	v_add_u32_e32 v16, v11, v16
	v_and_b32_e32 v13, 0xfc, v155
	v_and_b32_e32 v14, 56, v154
	s_mov_b32 s3, 6
	v_or_b32_e32 v4, 0x200, v10
	v_mov_b32_e32 v5, v3
	v_or_b32_e32 v6, 0x400, v10
	v_mov_b32_e32 v7, v3
	v_or_b32_e32 v8, 0x600, v10
	v_mov_b32_e32 v9, v3
	v_mov_b32_e32 v15, s12
	s_movk_i32 s13, 0x10b7
	s_movk_i32 s14, 0x800
	s_mov_b32 s15, 0x1104e000
	s_movk_i32 s16, -184
	v_add_u32_e32 v17, 0x404, v16
	v_add_u32_e32 v18, 0x40c, v16
	v_add_u32_e32 v19, 0x808, v16
	v_add_u32_e32 v20, 0xc0c, v16
	v_add_u32_e32 v21, 0xc14, v16
	v_add_u32_e32 v22, 0x1414, v16
	v_add_u32_e32 v23, 0x141c, v16
	v_add_u32_e32 v24, 0x1818, v16
	v_add_u32_e32 v25, 0x1c1c, v16
	v_add_u32_e32 v26, 0x1c24, v16
	v_lshlrev_b32_e32 v2, 1, v2
	v_add_u32_e32 v27, v27, v28
	v_lshlrev_b32_e32 v10, 1, v10
	s_branch .LBB0_782

; __device__ __forceinline__ void convert_deferred(const Ptrs& P, unsigned char* lds, int quota) {
;     const int tid = threadIdx.x, wid = tid >> 6, lane = tid & 63;
;     float* tile = (float*)lds;
;     volatile __attribute__((address_space(3))) int* slot = (volatile __attribute__((address_space(3))) int*)((__attribute__((address_space(3))) unsigned char*)lds + 131072 + 320 + 11000);
;     unsigned* q = (unsigned*)(P.ws + WS_CTL) + CW_DEFQ;
;     for (int n = 0; n < quota; ++n) {
;         __syncthreads();
;         if (tid == 0) *slot = (int)atomicAdd(q, 1u);
;         __syncthreads();
;         const int t = *slot;
;         if (t >= DEF_GU + DEF_DN) break;
;         const bool gu = t < DEF_GU;
;         const float* src = gu ? P.in[34] : P.in[36]; bf16* dst = (bf16*)(P.ws + (gu ? WS_WGU : WS_WDN));
;         const int N = gu ? 2048 : 1024, ntn = N / 256, it = gu ? 2 * NE * 16 * 8 - DEF_GU + t : 2 * NE * 16 * 4 - DEF_DN + (t - DEF_GU);
.LBB0_903:
	s_waitcnt vmcnt(0)
	s_barrier
	s_cmp_lt_u32 s2, 64
	s_cbranch_scc1 .Lcd3_skip
	v_lshlrev_b32_e32 v250, 2, v0
	v_lshlrev_b32_e32 v251, 3, v0
	s_waitcnt vmcnt(0) lgkmcnt(0)
	v_and_b32_e32 v186, 0x7c, v250
	v_lshlrev_b32_e32 v187, 5, v0
	s_movk_i32 s0, 0x400
	v_and_or_b32 v196, v187, s0, v186
	v_lshrrev_b32_e32 v186, 3, v0
	v_and_b32_e32 v198, 56, v186
	v_lshrrev_b32_e32 v186, 3, v182
	v_lshl_or_b32 v188, v1, 5, v186
	v_lshl_add_u32 v189, v182, 4, 0
	v_and_b32_e32 v186, 56, v251
	v_lshl_add_u32 v191, v188, 2, 0
	v_mul_u32_u24_e32 v195, 0x2020, v1
	v_lshlrev_b32_e32 v188, 6, v188
	v_mul_u32_u24_e32 v193, 0x404, v186
	v_or_b32_e32 v190, 0x200, v188
	v_or_b32_e32 v192, 0x400, v188
	v_or_b32_e32 v194, 0x600, v188
	s_add_i32 s10, 0, 0x22c38
	v_add_u32_e32 v200, v189, v195
	v_and_b32_e32 v197, 0xfc, v250
	s_mov_b32 s1, 0
	v_mov_b32_e32 v187, 0
	s_mov_b32 s3, 2
	v_mov_b32_e32 v199, s10
	s_movk_i32 s11, 0x10b7
	s_movk_i32 s80, 0x800
	s_mov_b32 s81, 0x1104e000
	s_movk_i32 s14, -184
	v_add_u32_e32 v201, 0x404, v200
	v_add_u32_e32 v202, 0x40c, v200
	v_add_u32_e32 v203, 0x808, v200
	v_add_u32_e32 v204, 0xc0c, v200
	v_add_u32_e32 v205, 0xc14, v200
	v_add_u32_e32 v206, 0x1414, v200
	v_add_u32_e32 v207, 0x141c, v200
	v_add_u32_e32 v208, 0x1818, v200
	v_add_u32_e32 v209, 0x1c1c, v200
	v_add_u32_e32 v210, 0x1c24, v200
	v_lshlrev_b32_e32 v186, 1, v186
	v_add_u32_e32 v211, v191, v193
	v_lshlrev_b32_e32 v188, 1, v188
	v_lshlrev_b32_e32 v190, 1, v190
	v_lshlrev_b32_e32 v192, 1, v192
	v_lshlrev_b32_e32 v194, 1, v194
	s_branch .Lcd3_2280

; __device__ __forceinline__ void convert_deferred(const Ptrs& P, unsigned char* lds, int quota) {
;     ...
;     for (int n = 0; n < quota; ++n) {
;         __syncthreads();
;         if (tid == 0) *slot = (int)atomicAdd(q, 1u);
;         __syncthreads();
.Lcd3_2280:
	s_waitcnt lgkmcnt(0)
	s_barrier
	s_mov_b64 s[4:5], exec
	v_readlane_b32 s6, v254, 22
	v_readlane_b32 s7, v254, 23
	s_and_b64 s[6:7], s[4:5], s[6:7]
	s_mov_b64 exec, s[6:7]
	s_cbranch_execz .Lcd3_2284
	s_mov_b64 s[8:9], exec
	v_mbcnt_lo_u32_b32 v189, s8, 0
	v_mbcnt_hi_u32_b32 v189, s9, v189
	v_cmp_eq_u32_e32 vcc, 0, v189

; __device__ __forceinline__ void convert_deferred(const Ptrs& P, unsigned char* lds, int quota) {
;     ...
;         if (tid == 0) *slot = (int)atomicAdd(q, 1u);
;         __syncthreads();
	s_and_saveexec_b64 s[6:7], vcc
	s_cbranch_execz .Lcd3_2283
	s_bcnt1_i32_b64 s0, s[8:9]
	v_mov_b32_e32 v191, s0
	global_atomic_add v191, v187, v191, s[78:79] offset:1024 sc0
.Lcd3_2283:
	s_or_b64 exec, exec, s[6:7]
	s_waitcnt vmcnt(0)
	v_readfirstlane_b32 s0, v191
	v_mov_b32_e32 v191, s10
	s_nop 0
	v_add_u32_e32 v189, s0, v189
	ds_write_b32 v191, v189
; __device__ __forceinline__ unsigned g8_cvt_pk(float lo, float hi) { unsigned r; asm volatile("v_cvt_pk_bf16_f32 %0, %1, %2" : "=v"(r) : "v"(lo), "v"(hi)); return r; }
; __device__ __forceinline__ void convert_deferred(const Ptrs& P, unsigned char* lds, int quota) {
;     ...
;         const int t = *slot;
;         if (t >= DEF_GU + DEF_DN) break;
;         const bool gu = t < DEF_GU;
;         const float* src = gu ? P.in[34] : P.in[36]; bf16* dst = (bf16*)(P.ws + (gu ? WS_WGU : WS_WDN));
;         const int N = gu ? 2048 : 1024, ntn = N / 256, it = gu ? 2 * NE * 16 * 8 - DEF_GU + t : 2 * NE * 16 * 4 - DEF_DN + (t - DEF_GU);
;         f32x4 cur[8];
;         bt_load(src, N, gu ? 1 : 0, it, ntn, cur);
; #pragma unroll
;         for (int i = 0; i < 8; ++i) { float* tp = tile + (wid * 8 + i) * 257 + lane * 4; tp[0] = cur[i][0]; tp[1] = cur[i][1]; tp[2] = cur[i][2]; tp[3] = cur[i][3]; }
;         __syncthreads();
;         const int per = 16 * ntn, z = it / per, r = it % per, kt = r / ntn, nt = r % ntn;
;         bf16* d = dst + (size_t)z * N * 1024 + (((size_t)nt * 16 + kt) << 14);
;         const int kc = lane & 7;
; #pragma unroll
;         for (int pss = 0; pss < 4; ++pss) {
;             const int nn = wid * 32 + pss * 8 + (lane >> 3); float f[8];
; #pragma unroll
;             for (int j = 0; j < 8; ++j) f[j] = tile[(kc * 8 + j) * 257 + nn];
;             u32x4 w; w.x = g8_cvt_pk(f[0], f[1]); w.y = g8_cvt_pk(f[2], f[3]); w.z = g8_cvt_pk(f[4], f[5]); w.w = g8_cvt_pk(f[6], f[7]);
;             *(u32x4*)(d + nn * 64 + kc * 8) = w;
;         }
.Lcd3_2284:
	s_or_b64 exec, exec, s[4:5]
	s_waitcnt lgkmcnt(0)
	s_barrier
	ds_read_b32 v189, v199
	s_mov_b64 s[4:5], -1
	s_waitcnt lgkmcnt(0)
	v_cmp_lt_i32_e32 vcc, s11, v189
	v_readfirstlane_b32 s0, v189
	s_cbranch_vccnz .Lcd3_2279
	s_cmpk_gt_i32 s0, 0xaef
	s_cselect_b64 vcc, -1, 0
	s_and_b64 s[4:5], vcc, exec
	s_cselect_b32 s4, s81, 0x104e000
	s_cselect_b32 s9, 0x400, s80
	s_cselect_b32 s15, s73, s69
	s_cselect_b32 s84, s72, s68
	s_cselect_b32 s5, s14, 0x1510
	s_cselect_b32 s82, 20, 21
	s_cselect_b32 s85, 10, 11
	s_add_u32 s86, s78, s4
	s_addc_u32 s87, s79, 0
	s_lshr_b32 s6, s9, 4
	s_abs_i32 s4, s6
	v_cvt_f32_u32_e32 v189, s4
	s_sub_i32 s83, 0, s4
	s_add_i32 s5, s5, s0
	s_abs_i32 s7, s5
	v_rcp_iflag_f32_e32 v189, v189
	s_xor_b32 s0, s5, s6
	s_lshr_b32 s8, s9, 8
	s_ashr_i32 s0, s0, 31
	v_mul_f32_e32 v189, 0x4f7ffffe, v189
	v_cvt_u32_f32_e32 v189, v189
	s_nop 0
	v_readfirstlane_b32 s88, v189
	s_mul_i32 s83, s83, s88
	s_mul_hi_u32 s83, s88, s83
	s_add_i32 s88, s88, s83
	s_mul_hi_u32 s83, s7, s88
	s_mul_i32 s88, s83, s4
	s_sub_i32 s7, s7, s88
	s_add_i32 s88, s83, 1
	s_sub_i32 s89, s7, s4
	s_cmp_ge_u32 s7, s4
	s_cselect_b32 s83, s88, s83
	s_cselect_b32 s7, s89, s7
	s_add_i32 s88, s83, 1
	s_cmp_ge_u32 s7, s4
	s_cselect_b32 s4, s88, s83
	s_xor_b32 s4, s4, s0
	s_sub_i32 s4, s4, s0
	s_sext_i32_i8 s0, s8
	v_cvt_f32_i32_e32 v189, s0
	s_mul_i32 s6, s4, s6
	s_sub_i32 s5, s5, s6
	v_cvt_f32_i32_e32 v191, s5
	v_rcp_iflag_f32_e32 v193, v189
	s_xor_b32 s0, s5, s0
	s_ashr_i32 s0, s0, 30
	s_or_b32 s0, s0, 1
	v_mul_f32_e32 v193, v191, v193
	v_trunc_f32_e32 v193, v193
	v_fma_f32 v191, -v193, v189, v191
	v_cvt_i32_f32_e32 v193, v193
	v_cmp_ge_f32_e64 s[6:7], |v191|, |v189|
	s_and_b64 s[6:7], s[6:7], exec
	s_cselect_b32 s0, s0, 0
	v_readfirstlane_b32 s6, v193
	s_add_i32 s6, s6, s0
	s_mul_i32 s7, s6, s8
	s_sub_i32 s8, s5, s7
	s_sext_i32_i8 s5, s8
	v_lshl_add_u32 v189, s5, 7, v196
	v_lshl_or_b32 v191, s5, 8, v197
	s_ashr_i32 s5, s4, 31
	s_sext_i32_i8 s0, s6
	s_lshl_b64 s[82:83], s[4:5], s82
	v_lshl_or_b32 v214, s0, 6, v198
	s_lshl_b64 s[82:83], s[82:83], 2
	v_ashrrev_i32_e32 v215, 31, v214
	s_add_u32 s82, s84, s82
	v_cndmask_b32_e32 v212, v189, v191, vcc
	s_addc_u32 s83, s15, s83
	v_lshlrev_b64 v[214:215], s85, v[214:215]
	v_lshl_add_u64 v[214:215], v[214:215], 2, s[82:83]
	v_ashrrev_i32_e32 v213, 31, v212
	v_lshl_add_u64 v[236:237], v[212:213], 2, v[214:215]
	s_lshl_b32 s0, s9, 2
	s_lshl_b64 s[82:83], 12, s85
	v_lshl_add_u64 v[220:221], v[236:237], 0, s[0:1]
	v_lshl_add_u64 v[228:229], v[236:237], 0, s[82:83]
	s_lshl_b64 s[82:83], 24, s85
	v_lshl_add_u64 v[238:239], v[220:221], 0, s[0:1]
	v_lshl_add_u64 v[240:241], v[236:237], 0, s[82:83]
	s_lshl_b64 s[82:83], 28, s85
	s_lshl_b32 s0, s9, 3
	v_lshl_add_u64 v[242:243], v[236:237], 0, s[82:83]
	v_lshl_add_u64 v[244:245], v[238:239], 0, s[0:1]
	s_lshl_b64 s[82:83], 20, s85
	global_load_dwordx4 v[212:215], v[236:237], off nt
	global_load_dwordx4 v[216:219], v[220:221], off nt
	s_nop 0
	global_load_dwordx4 v[220:223], v[238:239], off nt
	global_load_dwordx4 v[224:227], v[228:229], off nt
	s_nop 0
	global_load_dwordx4 v[228:231], v[240:241], off nt
	global_load_dwordx4 v[232:235], v[242:243], off nt
	v_lshl_add_u64 v[246:247], v[236:237], 0, s[82:83]
	global_load_dwordx4 v[236:239], v[244:245], off nt
	global_load_dwordx4 v[240:243], v[246:247], off nt
	s_lshl_b64 s[4:5], s[4:5], s85
	s_lshl_b64 s[4:5], s[4:5], 11
	s_add_u32 s0, s86, s4
	s_addc_u32 s9, s87, s5
	s_bfe_i64 s[4:5], s[8:9], 0x80000
	s_bfe_i64 s[6:7], s[6:7], 0x80000
	s_lshl_b64 s[4:5], s[4:5], 19
	s_add_u32 s0, s0, s4
	s_addc_u32 s8, s9, s5
	s_lshl_b64 s[4:5], s[6:7], 15
	s_add_u32 s4, s0, s4
	s_addc_u32 s5, s8, s5
	v_mov_b32_e32 v189, v187
	s_add_i32 s3, s3, -1
	s_cmp_eq_u32 s3, 0
	s_waitcnt vmcnt(7)
	ds_write_b128 v200, v[212:215]
	s_waitcnt vmcnt(6)
	ds_write2_b32 v201, v216, v217 offset1:1
	ds_write2_b32 v202, v218, v219 offset1:1
	s_waitcnt vmcnt(3)
	ds_write2_b64 v208, v[228:229], v[230:231] offset1:1
	s_waitcnt vmcnt(2)
	ds_write2_b32 v209, v232, v233 offset1:1
	ds_write2_b32 v210, v234, v235 offset1:1
	ds_write2_b64 v203, v[220:221], v[222:223] offset1:1
	ds_write2_b32 v204, v224, v225 offset1:1
	ds_write2_b32 v205, v226, v227 offset1:1
	s_waitcnt vmcnt(1)
	ds_write_b128 v200, v[236:239] offset:4112
	s_waitcnt vmcnt(0)
	ds_write2_b32 v206, v240, v241 offset1:1
	ds_write2_b32 v207, v242, v243 offset1:1
	s_waitcnt lgkmcnt(0)
	s_barrier
	ds_read_b32 v191, v211 offset:1028
	ds_read_b32 v193, v211 offset:3084
	ds_read_b32 v195, v211 offset:5140
	ds_read_b32 v215, v211 offset:7196
	ds_read_b32 v216, v211 offset:6168
	ds_read_b32 v214, v211 offset:4112
	ds_read_b32 v213, v211 offset:2056
	ds_read_b32 v212, v211
	s_waitcnt lgkmcnt(0)
	v_cvt_pk_bf16_f32 v212, v212, v191
	v_cvt_pk_bf16_f32 v213, v213, v193
	v_cvt_pk_bf16_f32 v214, v214, v195
	v_cvt_pk_bf16_f32 v215, v216, v215
	ds_read_b32 v191, v211 offset:1060
	ds_read_b32 v193, v211 offset:3116
	ds_read_b32 v195, v211 offset:5172
	ds_read_b32 v220, v211 offset:7228
	ds_read_b32 v221, v211 offset:6200
	ds_read_b32 v222, v211 offset:4144
	ds_read_b32 v223, v211 offset:2088
	ds_read_b32 v224, v211 offset:32
	v_lshl_add_u64 v[216:217], s[4:5], 0, v[186:187]
	v_lshl_add_u64 v[218:219], v[216:217], 0, v[188:189]
	global_store_dwordx4 v[218:219], v[212:215], off
	s_cselect_b64 s[4:5], -1, 0
	s_waitcnt lgkmcnt(0)
	v_cvt_pk_bf16_f32 v212, v224, v191
	v_cvt_pk_bf16_f32 v213, v223, v193
	v_cvt_pk_bf16_f32 v214, v222, v195
	v_cvt_pk_bf16_f32 v215, v221, v220
	ds_read_b32 v189, v211 offset:1092
	ds_read_b32 v193, v211 offset:3148
	ds_read_b32 v195, v211 offset:5204
	ds_read_b32 v220, v211 offset:6232
	ds_read_b32 v221, v211 offset:4176
	ds_read_b32 v222, v211 offset:2120
	ds_read_b32 v223, v211 offset:64
	ds_read_b32 v224, v211 offset:7260
	v_mov_b32_e32 v191, v187
	v_lshl_add_u64 v[218:219], v[216:217], 0, v[190:191]
	global_store_dwordx4 v[218:219], v[212:215], off
	s_waitcnt lgkmcnt(1)
	s_nop 0
	v_cvt_pk_bf16_f32 v212, v223, v189
	v_cvt_pk_bf16_f32 v213, v222, v193
	v_cvt_pk_bf16_f32 v214, v221, v195
	s_waitcnt lgkmcnt(0)
	v_cvt_pk_bf16_f32 v215, v220, v224
	ds_read_b32 v189, v211 offset:1124
	ds_read_b32 v191, v211 offset:3180
	ds_read_b32 v195, v211 offset:5236
	ds_read_b32 v220, v211 offset:6264
	ds_read_b32 v221, v211 offset:4208
	ds_read_b32 v222, v211 offset:2152
	ds_read_b32 v223, v211 offset:96
	ds_read_b32 v224, v211 offset:7292
	v_mov_b32_e32 v193, v187
	v_lshl_add_u64 v[218:219], v[216:217], 0, v[192:193]
	global_store_dwordx4 v[218:219], v[212:215], off
	s_waitcnt lgkmcnt(1)
	s_nop 0
	v_cvt_pk_bf16_f32 v212, v223, v189
	v_cvt_pk_bf16_f32 v213, v222, v191
	v_cvt_pk_bf16_f32 v214, v221, v195
	v_mov_b32_e32 v195, v187
	v_lshl_add_u64 v[216:217], v[216:217], 0, v[194:195]
	s_waitcnt lgkmcnt(0)
	v_cvt_pk_bf16_f32 v215, v220, v224
	global_store_dwordx4 v[216:217], v[212:215], off
	s_branch .Lcd3_2279

; __device__ __forceinline__ unsigned xb_add(unsigned* p, unsigned v) { return __hip_atomic_fetch_add(p, v, __ATOMIC_RELAXED, __HIP_MEMORY_SCOPE_AGENT); }
; __device__ __forceinline__ void xcd_barrier(const XcdBarrier& b) {
;     asm volatile("s_waitcnt vmcnt(0)" ::: "memory");
;     __syncthreads();
;     if (threadIdx.x == 0) {
;         unsigned* bar = b.bar;
;         __builtin_amdgcn_s_waitcnt(0);
;         unsigned nloc = b.st[0], nx = b.st[1];
;         if (nloc == 0u) { xcd_barrier_complete(bar, b.x, nloc, nx); b.st[0] = nloc; b.st[1] = nx; }
;         const unsigned old = xb_add(&bar[XB_XSUB(b.x)], 1u);
.Lcd3_skip:
.LBB0_904:
	s_cmp_gt_i32 s97, 4
	s_cselect_b64 s[0:1], -1, 0
	s_and_b64 s[4:5], s[12:13], s[0:1]
	s_andn2_b64 vcc, exec, s[4:5]
	s_cbranch_vccnz .LBB0_958
	s_waitcnt vmcnt(0)
	s_waitcnt vmcnt(0) lgkmcnt(0)
	s_barrier
	s_mov_b64 s[4:5], exec
	v_readlane_b32 s6, v254, 22
	v_readlane_b32 s7, v254, 23
	s_and_b64 s[6:7], s[4:5], s[6:7]
	s_mov_b64 exec, s[6:7]
	s_cbranch_execz .LBB0_957
	s_add_i32 s3, 0, 0x20160
	v_mov_b32_e32 v2, s3
	s_waitcnt vmcnt(0) expcnt(0) lgkmcnt(0)
	ds_read_b32 v4, v2
	s_add_i32 s3, 0, 0x20164
	v_mov_b32_e32 v2, s3
	ds_read_b32 v2, v2
	s_waitcnt lgkmcnt(1)
	v_cmp_ne_u32_e32 vcc, 0, v4
	s_cbranch_vccnz .LBB0_921
	v_readlane_b32 s6, v254, 0
	v_readlane_b32 s7, v254, 1
	s_load_dwordx2 s[10:11], s[6:7], 0x4
	s_add_u32 s6, s78, 0x4200
	s_addc_u32 s7, s79, 0
	s_add_u32 s8, s78, 0x4400
	s_addc_u32 s9, s79, 0
	s_waitcnt lgkmcnt(0)
	s_mul_i32 s3, s10, s62
	s_add_u32 s10, s78, 0x4500
	s_mul_i32 s3, s3, s11
	s_addc_u32 s11, s79, 0
	s_add_u32 s12, s78, 0x4600
	s_addc_u32 s13, s79, 0
	s_add_u32 s14, s78, 0x4700
	s_addc_u32 s15, s79, 0
	s_add_u32 s16, s78, 0x4800
	s_addc_u32 s17, s79, 0
	s_add_u32 s18, s78, 0x4900
	s_addc_u32 s19, s79, 0
	s_add_u32 s20, s78, 0x4a00
	s_addc_u32 s21, s79, 0
	s_add_u32 s26, s78, 0x4b00
	s_addc_u32 s27, s79, 0
	s_add_u32 s28, s78, 0x4c00
	s_addc_u32 s29, s79, 0
	s_add_u32 s30, s78, 0x4d00
	s_addc_u32 s31, s79, 0
	s_add_u32 s34, s78, 0x4e00
	s_addc_u32 s35, s79, 0
	s_add_u32 s36, s78, 0x4f00
	s_addc_u32 s37, s79, 0
	s_add_u32 s38, s78, 0x5000
	s_addc_u32 s39, s79, 0
	s_add_u32 s44, s78, 0x5100
	s_addc_u32 s45, s79, 0
	s_add_u32 s48, s78, 0x5200
	s_addc_u32 s49, s79, 0
	s_add_u32 s52, s78, 0x5300
	s_addc_u32 s53, s79, 0
	s_mov_b32 s33, 1
	v_mov_b32_e32 v18, 0
	s_branch .LBB0_909

; #define SEAM(k) do { if (IN(k) && IN((k) + 1)) xcd_barrier(bar); \
;         if (PROBE_MASK) { const unsigned long long t_ = __builtin_amdgcn_s_memrealtime(); if ((PROBE_MASK >> (k)) & 1u) pr_acc += t_ - pr_t0; pr_t0 = t_; } } while (0)
; __device__ __forceinline__ void convert_deferred(const Ptrs& P, unsigned char* lds, int quota) {
;     const int tid = threadIdx.x, wid = tid >> 6, lane = tid & 63;
;     float* tile = (float*)lds;
;     volatile __attribute__((address_space(3))) int* slot = (volatile __attribute__((address_space(3))) int*)((__attribute__((address_space(3))) unsigned char*)lds + 131072 + 320 + 11000);
;     unsigned* q = (unsigned*)(P.ws + WS_CTL) + CW_DEFQ;
;     for (int n = 0; n < quota; ++n) {
;         __syncthreads();
;         if (tid == 0) *slot = (int)atomicAdd(q, 1u);
;         __syncthreads();
;         const int t = *slot;
;         if (t >= DEF_GU + DEF_DN) break;
;         const bool gu = t < DEF_GU;
;         const float* src = gu ? P.in[34] : P.in[36]; bf16* dst = (bf16*)(P.ws + (gu ? WS_WGU : WS_WDN));
;         const int N = gu ? 2048 : 1024, ntn = N / 256, it = gu ? 2 * NE * 16 * 8 - DEF_GU + t : 2 * NE * 16 * 4 - DEF_DN + (t - DEF_GU);
; __global__ void __launch_bounds__(NT, 2) mega(Args args) {
;     ...
;     if (IN(6)) { g8::DenseOrder S; S.init(MIX, D, (const bf16*)(ws + WS_WEVOUT), D, R, D, G, (int)blockIdx.x, 0); g8::EpiOut E{P, 0};
;         g8::gemm_phase<g8::EpiOut, g8::DenseOrder, false, true>(LDSP, D, D, S, E);
;         if (IDLE_LAST(68 * 4)) convert_deferred(P, lds, 4); } SEAM(6);
.LBB0_1286:
	s_abs_i32 s3, s62
	v_cvt_f32_u32_e32 v2, s3
	s_sub_i32 s4, 0, s3
	s_mov_b32 s5, 0
	v_rcp_iflag_f32_e32 v2, v2
	s_nop 0
	v_mul_f32_e32 v2, 0x4f7ffffe, v2
	v_cvt_u32_f32_e32 v2, v2
	s_nop 0
	v_readfirstlane_b32 s6, v2
	s_mul_i32 s4, s4, s6
	s_mul_hi_u32 s4, s6, s4
	s_add_i32 s6, s6, s4
	s_mul_hi_u32 s4, s6, 0x110
	s_mul_i32 s4, s4, s3
	s_sub_i32 s4, 0x110, s4
	s_sub_i32 s6, s4, s3
	s_cmp_ge_u32 s4, s3
	s_cselect_b32 s4, s6, s4
	s_sub_i32 s6, s4, s3
	s_cmp_ge_u32 s4, s3
	s_cselect_b32 s3, s6, s4
	s_cmp_eq_u32 s3, 0
	s_cselect_b64 s[6:7], -1, 0
	s_cmp_lt_i32 s2, s3
	s_cselect_b64 s[8:9], -1, 0
	s_or_b64 s[6:7], s[6:7], s[8:9]
	s_and_b64 vcc, exec, s[6:7]
	s_cbranch_vccnz .LBB0_1296
	v_and_b32_e32 v2, 0x7c, v188
	v_lshlrev_b32_e32 v3, 5, v0
	s_movk_i32 s3, 0x400
	v_and_or_b32 v12, v3, s3, v2
	v_bfe_u32 v2, v0, 3, 3
	v_lshl_or_b32 v4, v1, 5, v2
	v_lshlrev_b32_e32 v2, 3, v0
	v_lshl_add_u32 v11, v182, 4, 0
	v_and_b32_e32 v2, 56, v2
	v_mul_u32_u24_e32 v16, 0x2020, v1
	v_mov_b32_e32 v3, 0
	v_lshl_add_u32 v27, v4, 2, 0
	v_mul_u32_u24_e32 v28, 0x404, v2
	v_lshlrev_b32_e32 v10, 6, v4
	s_add_i32 s12, 0, 0x22c38
	v_add_u32_e32 v16, v11, v16
	v_and_b32_e32 v13, 0xfc, v188
	v_and_b32_e32 v14, 56, v185
	s_mov_b32 s3, 8
	v_or_b32_e32 v4, 0x200, v10
	v_mov_b32_e32 v5, v3
	v_or_b32_e32 v6, 0x400, v10
	v_mov_b32_e32 v7, v3
	v_or_b32_e32 v8, 0x600, v10
	v_mov_b32_e32 v9, v3
	v_mov_b32_e32 v15, s12
	s_movk_i32 s13, 0x10b7
	s_movk_i32 s14, 0x800
	s_mov_b32 s15, 0x1104e000
	s_movk_i32 s16, -184
	v_add_u32_e32 v17, 0x404, v16
	v_add_u32_e32 v18, 0x40c, v16
	v_add_u32_e32 v19, 0x808, v16
	v_add_u32_e32 v20, 0xc0c, v16
	v_add_u32_e32 v21, 0xc14, v16
	v_add_u32_e32 v22, 0x1414, v16
	v_add_u32_e32 v23, 0x141c, v16
	v_add_u32_e32 v24, 0x1818, v16
	v_add_u32_e32 v25, 0x1c1c, v16
	v_add_u32_e32 v26, 0x1c24, v16
	v_lshlrev_b32_e32 v2, 1, v2
	v_add_u32_e32 v27, v27, v28
	v_lshlrev_b32_e32 v10, 1, v10
	s_branch .LBB0_1289

; #define LAS __attribute__((address_space(3)))
; #define SEAM(k) do { if (IN(k) && IN((k) + 1)) xcd_barrier(bar); \
;         if (PROBE_MASK) { const unsigned long long t_ = __builtin_amdgcn_s_memrealtime(); if ((PROBE_MASK >> (k)) & 1u) pr_acc += t_ - pr_t0; pr_t0 = t_; } } while (0)
; __device__ __forceinline__ void convert_deferred(const Ptrs& P, unsigned char* lds, int quota) {
;     const int tid = threadIdx.x, wid = tid >> 6, lane = tid & 63;
;     float* tile = (float*)lds;
;     volatile __attribute__((address_space(3))) int* slot = (volatile __attribute__((address_space(3))) int*)((__attribute__((address_space(3))) unsigned char*)lds + 131072 + 320 + 11000);
;     unsigned* q = (unsigned*)(P.ws + WS_CTL) + CW_DEFQ;
;     for (int n = 0; n < quota; ++n) {
;         __syncthreads();
;         if (tid == 0) *slot = (int)atomicAdd(q, 1u);
;         __syncthreads();
;         const int t = *slot;
;         if (t >= DEF_GU + DEF_DN) break;
;         const bool gu = t < DEF_GU;
;         const float* src = gu ? P.in[34] : P.in[36]; bf16* dst = (bf16*)(P.ws + (gu ? WS_WGU : WS_WDN));
;         const int N = gu ? 2048 : 1024, ntn = N / 256, it = gu ? 2 * NE * 16 * 8 - DEF_GU + t : 2 * NE * 16 * 4 - DEF_DN + (t - DEF_GU);
; __global__ void __launch_bounds__(NT, 2) mega(Args args) {
;     ...
;     if (IN(9)) { g8::MoeOrder S{(const char*)(ws + WS_ACT), (const char*)(ws + WS_WDN) + (size_t)0 * NE * 1024 * 1024 * 2, nullptr, (size_t)1024 * 1024 * 2, 4, D, G, vcu, 0, nullptr};
;         S.init((const unsigned*)(ws + WS_CTL) + CW_CNT + 0 * 64, (LAS int*)(LDSP + MISC_OFF + 256)); g8::EpiMoe2 E{P, 0}; g8::gemm_phase<g8::EpiMoe2, g8::MoeOrder, false, true>(LDSP, D, D, S, E);
;         { const int rem_ = ((LAS int*)(LDSP + MISC_OFF + 256))[96] % G; if (rem_ != 0 && vcu >= rem_) convert_deferred(P, lds, 5); } } SEAM(9);
.LBB0_1609:
	s_abs_i32 s0, s62
	v_cvt_f32_u32_e32 v2, s0
	s_sub_i32 s5, 0, s0
	s_abs_i32 s4, s9
	s_ashr_i32 s3, s9, 31
	v_rcp_iflag_f32_e32 v2, v2
	s_mov_b32 s1, 0
	v_mul_f32_e32 v2, 0x4f7ffffe, v2
	v_cvt_u32_f32_e32 v2, v2
	s_nop 0
	v_readfirstlane_b32 s6, v2
	s_mul_i32 s5, s5, s6
	s_mul_hi_u32 s5, s6, s5
	s_add_i32 s6, s6, s5
	s_mul_hi_u32 s5, s4, s6
	s_mul_i32 s5, s5, s0
	s_sub_i32 s4, s4, s5
	s_sub_i32 s5, s4, s0
	s_cmp_ge_u32 s4, s0
	s_cselect_b32 s4, s5, s4
	s_sub_i32 s5, s4, s0
	s_cmp_ge_u32 s4, s0
	s_cselect_b32 s0, s5, s4
	s_xor_b32 s0, s0, s3
	s_sub_i32 s0, s0, s3
	s_cmp_eq_u32 s0, 0
	v_readlane_b32 s3, v254, 2
	s_cselect_b64 s[4:5], -1, 0
	s_cmp_lt_i32 s3, s0
	s_cselect_b64 s[6:7], -1, 0
	s_or_b64 s[4:5], s[4:5], s[6:7]
	s_and_b64 vcc, exec, s[4:5]
	s_cbranch_vccnz .LBB0_1619
	v_and_b32_e32 v2, 0x7c, v175
	v_lshlrev_b32_e32 v3, 5, v0
	s_movk_i32 s0, 0x400
	v_and_or_b32 v12, v3, s0, v2
	v_bfe_u32 v2, v0, 3, 3
	v_lshl_or_b32 v4, v1, 5, v2
	v_lshlrev_b32_e32 v2, 3, v0
	v_lshl_add_u32 v11, v182, 4, 0
	v_and_b32_e32 v2, 56, v2
	v_mul_u32_u24_e32 v16, 0x2020, v1
	v_mov_b32_e32 v3, 0
	v_lshl_add_u32 v27, v4, 2, 0
	v_mul_u32_u24_e32 v28, 0x404, v2
	v_lshlrev_b32_e32 v10, 6, v4
	s_add_i32 s10, 0, 0x22c38
	v_add_u32_e32 v16, v11, v16
	s_mov_b32 s3, 7
	v_and_b32_e32 v13, 0xfc, v175
	v_and_b32_e32 v14, 56, v173
	v_or_b32_e32 v4, 0x200, v10
	v_mov_b32_e32 v5, v3
	v_or_b32_e32 v6, 0x400, v10
	v_mov_b32_e32 v7, v3
	v_or_b32_e32 v8, 0x600, v10
	v_mov_b32_e32 v9, v3
	v_mov_b32_e32 v15, s10
	s_movk_i32 s11, 0x10b7
	s_movk_i32 s12, 0x800
	s_mov_b32 s13, 0x1104e000
	s_movk_i32 s14, -184
	v_add_u32_e32 v17, 0x404, v16
	v_add_u32_e32 v18, 0x40c, v16
	v_add_u32_e32 v19, 0x808, v16
	v_add_u32_e32 v20, 0xc0c, v16
	v_add_u32_e32 v21, 0xc14, v16
	v_add_u32_e32 v22, 0x1414, v16
	v_add_u32_e32 v23, 0x141c, v16
	v_add_u32_e32 v24, 0x1818, v16
	v_add_u32_e32 v25, 0x1c1c, v16
	v_add_u32_e32 v26, 0x1c24, v16
	v_lshlrev_b32_e32 v2, 1, v2
	v_add_u32_e32 v27, v27, v28
	v_lshlrev_b32_e32 v10, 1, v10
	s_branch .LBB0_1612

; #define LAS __attribute__((address_space(3)))
; #define SEAM(k) do { if (IN(k) && IN((k) + 1)) xcd_barrier(bar); \
;         if (PROBE_MASK) { const unsigned long long t_ = __builtin_amdgcn_s_memrealtime(); if ((PROBE_MASK >> (k)) & 1u) pr_acc += t_ - pr_t0; pr_t0 = t_; } } while (0)
; __device__ __forceinline__ void convert_deferred(const Ptrs& P, unsigned char* lds, int quota) {
;     const int tid = threadIdx.x, wid = tid >> 6, lane = tid & 63;
;     float* tile = (float*)lds;
;     volatile __attribute__((address_space(3))) int* slot = (volatile __attribute__((address_space(3))) int*)((__attribute__((address_space(3))) unsigned char*)lds + 131072 + 320 + 11000);
;     unsigned* q = (unsigned*)(P.ws + WS_CTL) + CW_DEFQ;
;     for (int n = 0; n < quota; ++n) {
;         __syncthreads();
;         if (tid == 0) *slot = (int)atomicAdd(q, 1u);
;         __syncthreads();
;         const int t = *slot;
;         if (t >= DEF_GU + DEF_DN) break;
;         const bool gu = t < DEF_GU;
;         const float* src = gu ? P.in[34] : P.in[36]; bf16* dst = (bf16*)(P.ws + (gu ? WS_WGU : WS_WDN));
;         const int N = gu ? 2048 : 1024, ntn = N / 256, it = gu ? 2 * NE * 16 * 8 - DEF_GU + t : 2 * NE * 16 * 4 - DEF_DN + (t - DEF_GU);
; __global__ void __launch_bounds__(NT, 2) mega(Args args) {
;     ...
;     if (IN(11)) { g8::DenseOrder S; S.init(H, D, (const bf16*)(ws + WS_WODIN), D, R, ODD_IN, G, (int)blockIdx.x, 0);
;         g8::EpiDiffIn E{Z, P.in[25], P.in[26], (const float*)(ws + WS_ROPE), (const float*)(ws + WS_ROPE) + SEQ * 64, (LAS float*)(LDSP + MISC_OFF + 1024)};
;         g8::gemm_phase<g8::EpiDiffIn, g8::DenseOrder, false, true>(LDSP, D, D, S, E);
;         if (IDLE_LAST(68 * 12)) convert_deferred(P, lds, 4); } SEAM(11);
.LBB0_1851:
	s_abs_i32 s0, s62
	v_cvt_f32_u32_e32 v2, s0
	s_sub_i32 s3, 0, s0
	v_readlane_b32 s56, v254, 40
	s_mov_b32 s1, 0
	v_rcp_iflag_f32_e32 v2, v2
	v_readlane_b32 s57, v254, 41
	v_mul_f32_e32 v2, 0x4f7ffffe, v2
	v_cvt_u32_f32_e32 v2, v2
	s_nop 0
	v_readfirstlane_b32 s4, v2
	s_mul_i32 s3, s3, s4
	s_mul_hi_u32 s3, s4, s3
	s_add_i32 s4, s4, s3
	s_mul_hi_u32 s3, s4, 0x330
	s_mul_i32 s3, s3, s0
	s_sub_i32 s3, 0x330, s3
	s_sub_i32 s4, s3, s0
	s_cmp_ge_u32 s3, s0
	s_cselect_b32 s3, s4, s3
	s_sub_i32 s4, s3, s0
	s_cmp_ge_u32 s3, s0
	s_cselect_b32 s0, s4, s3
	s_cmp_eq_u32 s0, 0
	s_cselect_b64 s[4:5], -1, 0
	s_cmp_lt_i32 s2, s0
	s_cselect_b64 s[6:7], -1, 0
	s_or_b64 s[4:5], s[4:5], s[6:7]
	s_and_b64 vcc, exec, s[4:5]
	s_cbranch_vccnz .LBB0_1861
	v_and_b32_e32 v2, 0x7c, v218
	v_lshlrev_b32_e32 v3, 5, v0
	s_movk_i32 s0, 0x400
	v_and_or_b32 v12, v3, s0, v2
	v_bfe_u32 v2, v0, 3, 3
	v_lshl_or_b32 v4, v1, 5, v2
	v_lshlrev_b32_e32 v2, 3, v0
	v_lshl_add_u32 v11, v182, 4, 0
	v_and_b32_e32 v2, 56, v2
	v_mul_u32_u24_e32 v16, 0x2020, v1
	v_mov_b32_e32 v3, 0
	s_waitcnt vmcnt(0)
	v_lshl_add_u32 v27, v4, 2, 0
	v_mul_u32_u24_e32 v28, 0x404, v2
	v_lshlrev_b32_e32 v10, 6, v4
	s_add_i32 s10, 0, 0x22c38
	v_add_u32_e32 v16, v11, v16
	v_and_b32_e32 v13, 0xfc, v218
	v_and_b32_e32 v14, 56, v179
	s_mov_b32 s3, 8
	v_or_b32_e32 v4, 0x200, v10
	v_mov_b32_e32 v5, v3
	v_or_b32_e32 v6, 0x400, v10
	v_mov_b32_e32 v7, v3
	v_or_b32_e32 v8, 0x600, v10
	v_mov_b32_e32 v9, v3
	v_mov_b32_e32 v15, s10
	s_movk_i32 s11, 0x10b7
	s_movk_i32 s12, 0x800
	s_mov_b32 s13, 0x1104e000
	s_movk_i32 s14, -184
	v_add_u32_e32 v17, 0x404, v16
	v_add_u32_e32 v18, 0x40c, v16
	v_add_u32_e32 v19, 0x808, v16
	v_add_u32_e32 v20, 0xc0c, v16
	v_add_u32_e32 v21, 0xc14, v16
	v_add_u32_e32 v22, 0x1414, v16
	v_add_u32_e32 v23, 0x141c, v16
	v_add_u32_e32 v24, 0x1818, v16
	v_add_u32_e32 v25, 0x1c1c, v16
	v_add_u32_e32 v26, 0x1c24, v16
	v_lshlrev_b32_e32 v2, 1, v2
	v_add_u32_e32 v27, v27, v28
	v_lshlrev_b32_e32 v10, 1, v10
	s_branch .LBB0_1854

; #define SEAM(k) do { if (IN(k) && IN((k) + 1)) xcd_barrier(bar); \
;         if (PROBE_MASK) { const unsigned long long t_ = __builtin_amdgcn_s_memrealtime(); if ((PROBE_MASK >> (k)) & 1u) pr_acc += t_ - pr_t0; pr_t0 = t_; } } while (0)
; __device__ __forceinline__ void convert_deferred(const Ptrs& P, unsigned char* lds, int quota) {
;     const int tid = threadIdx.x, wid = tid >> 6, lane = tid & 63;
;     float* tile = (float*)lds;
;     volatile __attribute__((address_space(3))) int* slot = (volatile __attribute__((address_space(3))) int*)((__attribute__((address_space(3))) unsigned char*)lds + 131072 + 320 + 11000);
;     unsigned* q = (unsigned*)(P.ws + WS_CTL) + CW_DEFQ;
;     for (int n = 0; n < quota; ++n) {
;         __syncthreads();
;         if (tid == 0) *slot = (int)atomicAdd(q, 1u);
;         __syncthreads();
;         const int t = *slot;
;         if (t >= DEF_GU + DEF_DN) break;
;         const bool gu = t < DEF_GU;
;         const float* src = gu ? P.in[34] : P.in[36]; bf16* dst = (bf16*)(P.ws + (gu ? WS_WGU : WS_WDN));
;         const int N = gu ? 2048 : 1024, ntn = N / 256, it = gu ? 2 * NE * 16 * 8 - DEF_GU + t : 2 * NE * 16 * 4 - DEF_DN + (t - DEF_GU);
; __global__ void __launch_bounds__(NT, 2) mega(Args args) {
;     ...
;     if (IN(15)) { ph_norm2_router(P, lds, 1, 1); convert_deferred(P, lds, 1 << 20); } SEAM(15);
.LBB0_2278:
	v_and_b32_e32 v2, 0x7c, v179
	v_lshlrev_b32_e32 v3, 5, v0
	s_movk_i32 s0, 0x400
	v_and_or_b32 v12, v3, s0, v2
	v_lshrrev_b32_e32 v2, 3, v0
	v_and_b32_e32 v14, 56, v2
	v_lshrrev_b32_e32 v2, 3, v182
	v_lshl_or_b32 v4, v1, 5, v2
	v_lshl_add_u32 v5, v182, 4, 0
	v_and_b32_e32 v2, 56, v188
	v_lshl_add_u32 v7, v4, 2, 0
	v_mul_u32_u24_e32 v11, 0x2020, v1
	v_lshlrev_b32_e32 v4, 6, v4
	v_mul_u32_u24_e32 v9, 0x404, v2
	v_or_b32_e32 v6, 0x200, v4
	v_or_b32_e32 v8, 0x400, v4
	v_or_b32_e32 v10, 0x600, v4
	s_add_i32 s10, 0, 0x22c38
	v_add_u32_e32 v16, v5, v11
	v_and_b32_e32 v13, 0xfc, v179
	s_mov_b32 s1, 0
	v_mov_b32_e32 v3, 0
	s_mov_b32 s3, 0x100000
	v_mov_b32_e32 v15, s10
	s_movk_i32 s11, 0x10b7
	s_movk_i32 s12, 0x800
	s_mov_b32 s13, 0x1104e000
	s_movk_i32 s14, -184
	v_add_u32_e32 v17, 0x404, v16
	v_add_u32_e32 v18, 0x40c, v16
	v_add_u32_e32 v19, 0x808, v16
	v_add_u32_e32 v20, 0xc0c, v16
	v_add_u32_e32 v21, 0xc14, v16
	v_add_u32_e32 v22, 0x1414, v16
	v_add_u32_e32 v23, 0x141c, v16
	v_add_u32_e32 v24, 0x1818, v16
	v_add_u32_e32 v25, 0x1c1c, v16
	v_add_u32_e32 v26, 0x1c24, v16
	v_lshlrev_b32_e32 v2, 1, v2
	v_add_u32_e32 v27, v7, v9
	v_lshlrev_b32_e32 v4, 1, v4
	v_lshlrev_b32_e32 v6, 1, v6
	v_lshlrev_b32_e32 v8, 1, v8
	v_lshlrev_b32_e32 v10, 1, v10
	s_branch .LBB0_2280
